# speedup vs baseline: 1.0631x; 1.0025x over previous
.LBB0_21:
	v_exp_f32_e64 v156, -|v154|
	v_max_f32 v157, 0, v154
	v_add_f32 v156, 1.0, v156
	v_log_f32 v156, v156
	s_nop 0
	v_fma_mixlo_f16 v155, v156, 1.0, v157
	ds_write_b16 v148, v155
	v_mov_b32_e32 v192, v106
	v_mov_b32_e32 v193, 0
	v_mov_b32_e32 v196, v110
	v_mov_b32_e32 v197, 0
	v_mul_f32 v182, -2.0, v153
	s_waitcnt lgkmcnt(0)
	s_barrier
	ds_read_b128 v[216:219], v139
	s_nop 4
	ds_read_b128 v[220:223], v141
	s_waitcnt lgkmcnt(1)
	v_smfmac_f32_16x16x64_f16 v[192:195], v[216:219], v[6:13], v191
	v_smfmac_f32_16x16x64_f16 v[196:199], v[216:219], v[26:33], v191
	s_waitcnt lgkmcnt(0)
	v_smfmac_f32_16x16x64_f16 v[192:195], v[220:223], v[14:21], v191
	v_smfmac_f32_16x16x64_f16 v[196:199], v[220:223], v[34:41], v191
	s_nop 6
	v_add_f32_e32 v224, v192, v193
	v_add_f32_e32 v225, v196, v197
	v_cndmask_b32_e64 v154, v224, v225, s[0:1]
	v_exp_f32_e64 v156, -|v154|
	v_max_f32 v157, 0, v154
	v_add_f32 v156, 1.0, v156
	v_log_f32 v156, v156
	s_nop 0
	v_fma_mixlo_f16 v155, v156, 1.0, v157
	ds_write_b16 v149, v155
	v_mov_b32_e32 v200, v114
	v_mov_b32_e32 v201, 0
	v_mov_b32_e32 v204, v118
	v_mov_b32_e32 v205, 0
	v_mov_b32_e32 v208, v122
	v_mov_b32_e32 v209, 0
	v_mov_b32_e32 v212, v126
	v_mov_b32_e32 v213, 0
	s_waitcnt lgkmcnt(0)
	s_barrier
	ds_read_b128 v[216:219], v143
	s_nop 4
	ds_read_b128 v[220:223], v145
	s_waitcnt lgkmcnt(1)
	v_smfmac_f32_16x16x64_f16 v[200:203], v[216:219], v[42:49], v191
	v_smfmac_f32_16x16x64_f16 v[204:207], v[216:219], v[58:65], v191
	v_smfmac_f32_16x16x64_f16 v[208:211], v[216:219], v[74:81], v191
	v_smfmac_f32_16x16x64_f16 v[212:215], v[216:219], v[90:97], v191
	s_waitcnt lgkmcnt(0)
	v_smfmac_f32_16x16x64_f16 v[200:203], v[220:223], v[50:57], v191
	v_smfmac_f32_16x16x64_f16 v[204:207], v[220:223], v[66:73], v191
	v_smfmac_f32_16x16x64_f16 v[208:211], v[220:223], v[82:89], v191
	v_smfmac_f32_16x16x64_f16 v[212:215], v[220:223], v[98:105], v191
	s_nop 4
	v_add_f32_e32 v224, v200, v201
	v_add_f32_e32 v225, v204, v205
	v_add_f32_e32 v226, v208, v209
	v_add_f32_e32 v227, v212, v213
	v_cndmask_b32_e64 v170, v225, v224, s[6:7]
	v_cndmask_b32_e64 v170, v170, v226, s[0:1]
	v_cndmask_b32_e64 v170, v170, v227, s[4:5]
	v_exp_f32_e32 v170, v170
	s_nop 0
	v_add_f32_e32 v170, 1.0, v170
	v_rcp_f32_e32 v170, v170
	s_nop 0
	v_fmac_f32_e32 v153, v170, v182
	s_nop 1
	v_add_f32_dpp v153, v153, v153 quad_perm:[1,0,3,2] row_mask:0xf bank_mask:0xf bound_ctrl:1
	s_nop 1
	v_add_f32_dpp v153, v153, v153 quad_perm:[2,3,0,1] row_mask:0xf bank_mask:0xf bound_ctrl:1
	s_nop 1
	v_add_f32_dpp v153, v153, v153 row_half_mirror row_mask:0xf bank_mask:0xf bound_ctrl:1
	v_cvt_f16_f32_e32 v170, v153
	ds_write_b16 v150, v170
	s_waitcnt lgkmcnt(0)
	s_barrier
	ds_read_b128 v[154:157], v147
	s_waitcnt lgkmcnt(0)
	v_mfma_f32_16x16x32_f16 v[130:133], v[154:157], v[2:5], v[130:133]
	v_mfma_f32_16x16x32_f16 v[154:157], v[154:157], v[22:25], v[134:137]
	s_nop 2
	v_add_u32_e32 v134, s3, v151
	ds_read_b32 v135, v134
	s_nop 2
	v_cndmask_b32_e64 v136, v130, v154, s[0:1]
	v_exp_f32_e64 v158, -|v136|
	v_max_f32 v159, 0, v136
	v_add_f32 v158, 1.0, v158
	v_log_f32 v158, v158
	s_nop 0
	v_fma_mixlo_f16 v137, v158, 1.0, v159
	ds_write_b16 v148, v137
	v_mov_b32_e32 v192, v106
	v_mov_b32_e32 v193, 0
	v_mov_b32_e32 v196, v110
	v_mov_b32_e32 v197, 0
	v_add_f32_e32 v136, v152, v153
	v_mul_f32 v137, -2.0, v135
	s_waitcnt lgkmcnt(0)
	s_barrier
	ds_read_b128 v[216:219], v139
	s_nop 4
	ds_read_b128 v[220:223], v141
	s_waitcnt lgkmcnt(1)
	v_smfmac_f32_16x16x64_f16 v[192:195], v[216:219], v[6:13], v191
	v_smfmac_f32_16x16x64_f16 v[196:199], v[216:219], v[26:33], v191
	s_waitcnt lgkmcnt(0)
	v_smfmac_f32_16x16x64_f16 v[192:195], v[220:223], v[14:21], v191
	v_smfmac_f32_16x16x64_f16 v[196:199], v[220:223], v[34:41], v191
	s_nop 6
	v_add_f32_e32 v224, v192, v193
	v_add_f32_e32 v225, v196, v197
	v_cndmask_b32_e64 v152, v224, v225, s[0:1]
	v_exp_f32_e64 v158, -|v152|
	v_max_f32 v159, 0, v152
	v_add_f32 v158, 1.0, v158
	v_log_f32 v158, v158
	s_nop 0
	v_fma_mixlo_f16 v153, v158, 1.0, v159
	ds_write_b16 v149, v153
	v_mov_b32_e32 v200, v114
	v_mov_b32_e32 v201, 0
	v_mov_b32_e32 v204, v118
	v_mov_b32_e32 v205, 0
	v_mov_b32_e32 v208, v122
	v_mov_b32_e32 v209, 0
	v_mov_b32_e32 v212, v126
	v_mov_b32_e32 v213, 0
	s_waitcnt lgkmcnt(0)
	s_barrier
	ds_read_b128 v[216:219], v143
	s_nop 4
	ds_read_b128 v[220:223], v145
	s_waitcnt lgkmcnt(1)
	v_smfmac_f32_16x16x64_f16 v[200:203], v[216:219], v[42:49], v191
	v_smfmac_f32_16x16x64_f16 v[204:207], v[216:219], v[58:65], v191
	v_smfmac_f32_16x16x64_f16 v[208:211], v[216:219], v[74:81], v191
	v_smfmac_f32_16x16x64_f16 v[212:215], v[216:219], v[90:97], v191
	s_waitcnt lgkmcnt(0)
	v_smfmac_f32_16x16x64_f16 v[200:203], v[220:223], v[50:57], v191
	v_smfmac_f32_16x16x64_f16 v[204:207], v[220:223], v[66:73], v191
	v_smfmac_f32_16x16x64_f16 v[208:211], v[220:223], v[82:89], v191
	v_smfmac_f32_16x16x64_f16 v[212:215], v[220:223], v[98:105], v191
	s_nop 4
	v_add_f32_e32 v224, v200, v201
	v_add_f32_e32 v225, v204, v205
	v_add_f32_e32 v226, v208, v209
	v_add_f32_e32 v227, v212, v213
	v_cndmask_b32_e64 v152, v225, v224, s[6:7]
	v_cndmask_b32_e64 v152, v152, v226, s[0:1]
	v_cndmask_b32_e64 v152, v152, v227, s[4:5]
	v_exp_f32_e32 v152, v152
	s_nop 0
	v_add_f32_e32 v152, 1.0, v152
	v_rcp_f32_e32 v152, v152
	s_nop 0
	v_fmac_f32_e32 v135, v152, v137
	s_nop 1
	v_add_f32_dpp v135, v135, v135 quad_perm:[1,0,3,2] row_mask:0xf bank_mask:0xf bound_ctrl:1
	s_nop 1
	v_add_f32_dpp v135, v135, v135 quad_perm:[2,3,0,1] row_mask:0xf bank_mask:0xf bound_ctrl:1
	s_nop 1
	v_add_f32_dpp v135, v135, v135 row_half_mirror row_mask:0xf bank_mask:0xf bound_ctrl:1
	v_cvt_f16_f32_e32 v137, v135
	ds_write_b16 v150, v137
	v_add_f32_e32 v135, v136, v135
	s_waitcnt lgkmcnt(0)
	s_barrier
	ds_read_b128 v[158:161], v147
	ds_read_b32 v137, v134 offset:32
	s_waitcnt lgkmcnt(1)
	v_mfma_f32_16x16x32_f16 v[130:133], v[158:161], v[2:5], v[130:133]
	v_mfma_f32_16x16x32_f16 v[152:155], v[158:161], v[22:25], v[154:157]
	s_nop 7
	v_cndmask_b32_e64 v156, v130, v152, s[0:1]
	v_exp_f32_e64 v158, -|v156|
	v_max_f32 v159, 0, v156
	v_add_f32 v158, 1.0, v158
	v_log_f32 v158, v158
	s_nop 0
	v_fma_mixlo_f16 v157, v158, 1.0, v159
	ds_write_b16 v148, v157
	v_mov_b32_e32 v192, v106
	v_mov_b32_e32 v193, 0
	v_mov_b32_e32 v196, v110
	v_mov_b32_e32 v197, 0
	v_mul_f32 v136, -2.0, v137
	s_waitcnt lgkmcnt(0)
	s_barrier
	ds_read_b128 v[216:219], v139
	s_nop 4
	ds_read_b128 v[220:223], v141
	s_waitcnt lgkmcnt(1)
	v_smfmac_f32_16x16x64_f16 v[192:195], v[216:219], v[6:13], v191
	v_smfmac_f32_16x16x64_f16 v[196:199], v[216:219], v[26:33], v191
	s_waitcnt lgkmcnt(0)
	v_smfmac_f32_16x16x64_f16 v[192:195], v[220:223], v[14:21], v191
	v_smfmac_f32_16x16x64_f16 v[196:199], v[220:223], v[34:41], v191
	s_nop 6
	v_add_f32_e32 v224, v192, v193
	v_add_f32_e32 v225, v196, v197
	v_cndmask_b32_e64 v156, v224, v225, s[0:1]
	v_exp_f32_e64 v158, -|v156|
	v_max_f32 v159, 0, v156
	v_add_f32 v158, 1.0, v158
	v_log_f32 v158, v158
	s_nop 0
	v_fma_mixlo_f16 v157, v158, 1.0, v159
	ds_write_b16 v149, v157
	v_mov_b32_e32 v200, v114
	v_mov_b32_e32 v201, 0
	v_mov_b32_e32 v204, v118
	v_mov_b32_e32 v205, 0
	v_mov_b32_e32 v208, v122
	v_mov_b32_e32 v209, 0
	v_mov_b32_e32 v212, v126
	v_mov_b32_e32 v213, 0
	s_waitcnt lgkmcnt(0)
	s_barrier
	ds_read_b128 v[216:219], v143
	s_nop 4
	ds_read_b128 v[220:223], v145
	s_waitcnt lgkmcnt(1)
	v_smfmac_f32_16x16x64_f16 v[200:203], v[216:219], v[42:49], v191
	v_smfmac_f32_16x16x64_f16 v[204:207], v[216:219], v[58:65], v191
	v_smfmac_f32_16x16x64_f16 v[208:211], v[216:219], v[74:81], v191
	v_smfmac_f32_16x16x64_f16 v[212:215], v[216:219], v[90:97], v191
	s_waitcnt lgkmcnt(0)
	v_smfmac_f32_16x16x64_f16 v[200:203], v[220:223], v[50:57], v191
	v_smfmac_f32_16x16x64_f16 v[204:207], v[220:223], v[66:73], v191
	v_smfmac_f32_16x16x64_f16 v[208:211], v[220:223], v[82:89], v191
	v_smfmac_f32_16x16x64_f16 v[212:215], v[220:223], v[98:105], v191
	s_nop 4
	v_add_f32_e32 v224, v200, v201
	v_add_f32_e32 v225, v204, v205
	v_add_f32_e32 v226, v208, v209
	v_add_f32_e32 v227, v212, v213
	v_cndmask_b32_e64 v172, v225, v224, s[6:7]
	v_cndmask_b32_e64 v172, v172, v226, s[0:1]
	v_cndmask_b32_e64 v172, v172, v227, s[4:5]
	v_exp_f32_e32 v172, v172
	s_nop 0
	v_add_f32_e32 v172, 1.0, v172
	v_rcp_f32_e32 v172, v172
	s_nop 0
	v_fmac_f32_e32 v137, v172, v136
	s_nop 1
	v_add_f32_dpp v136, v137, v137 quad_perm:[1,0,3,2] row_mask:0xf bank_mask:0xf bound_ctrl:1
	s_nop 1
	v_add_f32_dpp v136, v136, v136 quad_perm:[2,3,0,1] row_mask:0xf bank_mask:0xf bound_ctrl:1
	s_nop 1
	v_add_f32_dpp v136, v136, v136 row_half_mirror row_mask:0xf bank_mask:0xf bound_ctrl:1
	v_cvt_f16_f32_e32 v137, v136
	ds_write_b16 v150, v137
	v_add_f32_e32 v135, v135, v136
	s_waitcnt lgkmcnt(0)
	s_barrier
	ds_read_b128 v[156:159], v147
	ds_read_b32 v137, v134 offset:64
	s_waitcnt lgkmcnt(1)
	v_mfma_f32_16x16x32_f16 v[130:133], v[156:159], v[2:5], v[130:133]
	v_mfma_f32_16x16x32_f16 v[152:155], v[156:159], v[22:25], v[152:155]
	s_nop 7
	v_cndmask_b32_e64 v156, v130, v152, s[0:1]
	v_exp_f32_e64 v158, -|v156|
	v_max_f32 v159, 0, v156
	v_add_f32 v158, 1.0, v158
	v_log_f32 v158, v158
	s_nop 0
	v_fma_mixlo_f16 v157, v158, 1.0, v159
	ds_write_b16 v148, v157
	v_mov_b32_e32 v192, v106
	v_mov_b32_e32 v193, 0
	v_mov_b32_e32 v196, v110
	v_mov_b32_e32 v197, 0
	v_mul_f32 v136, -2.0, v137
	s_waitcnt lgkmcnt(0)
	s_barrier
	ds_read_b128 v[216:219], v139
	s_nop 4
	ds_read_b128 v[220:223], v141
	s_waitcnt lgkmcnt(1)
	v_smfmac_f32_16x16x64_f16 v[192:195], v[216:219], v[6:13], v191
	v_smfmac_f32_16x16x64_f16 v[196:199], v[216:219], v[26:33], v191
	s_waitcnt lgkmcnt(0)
	v_smfmac_f32_16x16x64_f16 v[192:195], v[220:223], v[14:21], v191
	v_smfmac_f32_16x16x64_f16 v[196:199], v[220:223], v[34:41], v191
	s_nop 6
	v_add_f32_e32 v224, v192, v193
	v_add_f32_e32 v225, v196, v197
	v_cndmask_b32_e64 v156, v224, v225, s[0:1]
	v_exp_f32_e64 v158, -|v156|
	v_max_f32 v159, 0, v156
	v_add_f32 v158, 1.0, v158
	v_log_f32 v158, v158
	s_nop 0
	v_fma_mixlo_f16 v157, v158, 1.0, v159
	ds_write_b16 v149, v157
	v_mov_b32_e32 v200, v114
	v_mov_b32_e32 v201, 0
	v_mov_b32_e32 v204, v118
	v_mov_b32_e32 v205, 0
	v_mov_b32_e32 v208, v122
	v_mov_b32_e32 v209, 0
	v_mov_b32_e32 v212, v126
	v_mov_b32_e32 v213, 0
	s_waitcnt lgkmcnt(0)
	s_barrier
	ds_read_b128 v[216:219], v143
	s_nop 4
	ds_read_b128 v[220:223], v145
	s_waitcnt lgkmcnt(1)
	v_smfmac_f32_16x16x64_f16 v[200:203], v[216:219], v[42:49], v191
	v_smfmac_f32_16x16x64_f16 v[204:207], v[216:219], v[58:65], v191
	v_smfmac_f32_16x16x64_f16 v[208:211], v[216:219], v[74:81], v191
	v_smfmac_f32_16x16x64_f16 v[212:215], v[216:219], v[90:97], v191
	s_waitcnt lgkmcnt(0)
	v_smfmac_f32_16x16x64_f16 v[200:203], v[220:223], v[50:57], v191
	v_smfmac_f32_16x16x64_f16 v[204:207], v[220:223], v[66:73], v191
	v_smfmac_f32_16x16x64_f16 v[208:211], v[220:223], v[82:89], v191
	v_smfmac_f32_16x16x64_f16 v[212:215], v[220:223], v[98:105], v191
	s_nop 4
	v_add_f32_e32 v224, v200, v201
	v_add_f32_e32 v225, v204, v205
	v_add_f32_e32 v226, v208, v209
	v_add_f32_e32 v227, v212, v213
	v_cndmask_b32_e64 v172, v225, v224, s[6:7]
	v_cndmask_b32_e64 v172, v172, v226, s[0:1]
	v_cndmask_b32_e64 v172, v172, v227, s[4:5]
	v_exp_f32_e32 v172, v172
	s_nop 0
	v_add_f32_e32 v172, 1.0, v172
	v_rcp_f32_e32 v172, v172
	s_nop 0
	v_fmac_f32_e32 v137, v172, v136
	s_nop 1
	v_add_f32_dpp v136, v137, v137 quad_perm:[1,0,3,2] row_mask:0xf bank_mask:0xf bound_ctrl:1
	s_nop 1
	v_add_f32_dpp v136, v136, v136 quad_perm:[2,3,0,1] row_mask:0xf bank_mask:0xf bound_ctrl:1
	s_nop 1
	v_add_f32_dpp v136, v136, v136 row_half_mirror row_mask:0xf bank_mask:0xf bound_ctrl:1
	v_cvt_f16_f32_e32 v137, v136
	ds_write_b16 v150, v137
	v_add_f32_e32 v135, v135, v136
	s_waitcnt lgkmcnt(0)
	s_barrier
	ds_read_b128 v[156:159], v147
	ds_read_b32 v137, v134 offset:96
	s_waitcnt lgkmcnt(1)
	v_mfma_f32_16x16x32_f16 v[130:133], v[156:159], v[2:5], v[130:133]
	v_mfma_f32_16x16x32_f16 v[152:155], v[156:159], v[22:25], v[152:155]
	s_nop 7
	v_cndmask_b32_e64 v156, v130, v152, s[0:1]
	v_exp_f32_e64 v158, -|v156|
	v_max_f32 v159, 0, v156
	v_add_f32 v158, 1.0, v158
	v_log_f32 v158, v158
	s_nop 0
	v_fma_mixlo_f16 v157, v158, 1.0, v159
	ds_write_b16 v148, v157
	v_mov_b32_e32 v192, v106
	v_mov_b32_e32 v193, 0
	v_mov_b32_e32 v196, v110
	v_mov_b32_e32 v197, 0
	v_mul_f32 v136, -2.0, v137
	s_waitcnt lgkmcnt(0)
	s_barrier
	ds_read_b128 v[216:219], v139
	s_nop 4
	ds_read_b128 v[220:223], v141
	s_waitcnt lgkmcnt(1)
	v_smfmac_f32_16x16x64_f16 v[192:195], v[216:219], v[6:13], v191
	v_smfmac_f32_16x16x64_f16 v[196:199], v[216:219], v[26:33], v191
	s_waitcnt lgkmcnt(0)
	v_smfmac_f32_16x16x64_f16 v[192:195], v[220:223], v[14:21], v191
	v_smfmac_f32_16x16x64_f16 v[196:199], v[220:223], v[34:41], v191
	s_nop 6
	v_add_f32_e32 v224, v192, v193
	v_add_f32_e32 v225, v196, v197
	v_cndmask_b32_e64 v156, v224, v225, s[0:1]
	v_exp_f32_e64 v158, -|v156|
	v_max_f32 v159, 0, v156
	v_add_f32 v158, 1.0, v158
	v_log_f32 v158, v158
	s_nop 0
	v_fma_mixlo_f16 v157, v158, 1.0, v159
	ds_write_b16 v149, v157
	v_mov_b32_e32 v200, v114
	v_mov_b32_e32 v201, 0
	v_mov_b32_e32 v204, v118
	v_mov_b32_e32 v205, 0
	v_mov_b32_e32 v208, v122
	v_mov_b32_e32 v209, 0
	v_mov_b32_e32 v212, v126
	v_mov_b32_e32 v213, 0
	s_waitcnt lgkmcnt(0)
	s_barrier
	ds_read_b128 v[216:219], v143
	s_nop 4
	ds_read_b128 v[220:223], v145
	s_waitcnt lgkmcnt(1)
	v_smfmac_f32_16x16x64_f16 v[200:203], v[216:219], v[42:49], v191
	v_smfmac_f32_16x16x64_f16 v[204:207], v[216:219], v[58:65], v191
	v_smfmac_f32_16x16x64_f16 v[208:211], v[216:219], v[74:81], v191
	v_smfmac_f32_16x16x64_f16 v[212:215], v[216:219], v[90:97], v191
	s_waitcnt lgkmcnt(0)
	v_smfmac_f32_16x16x64_f16 v[200:203], v[220:223], v[50:57], v191
	v_smfmac_f32_16x16x64_f16 v[204:207], v[220:223], v[66:73], v191
	v_smfmac_f32_16x16x64_f16 v[208:211], v[220:223], v[82:89], v191
	v_smfmac_f32_16x16x64_f16 v[212:215], v[220:223], v[98:105], v191
	s_nop 4
	v_add_f32_e32 v224, v200, v201
	v_add_f32_e32 v225, v204, v205
	v_add_f32_e32 v226, v208, v209
	v_add_f32_e32 v227, v212, v213
	v_cndmask_b32_e64 v172, v225, v224, s[6:7]
	v_cndmask_b32_e64 v172, v172, v226, s[0:1]
	v_cndmask_b32_e64 v172, v172, v227, s[4:5]
	v_exp_f32_e32 v172, v172
	s_nop 0
	v_add_f32_e32 v172, 1.0, v172
	v_rcp_f32_e32 v172, v172
	s_nop 0
	v_fmac_f32_e32 v137, v172, v136
	s_nop 1
	v_add_f32_dpp v136, v137, v137 quad_perm:[1,0,3,2] row_mask:0xf bank_mask:0xf bound_ctrl:1
	s_nop 1
	v_add_f32_dpp v136, v136, v136 quad_perm:[2,3,0,1] row_mask:0xf bank_mask:0xf bound_ctrl:1
	s_nop 1
	v_add_f32_dpp v136, v136, v136 row_half_mirror row_mask:0xf bank_mask:0xf bound_ctrl:1
	v_cvt_f16_f32_e32 v137, v136
	ds_write_b16 v150, v137
	v_add_f32_e32 v135, v135, v136
	s_waitcnt lgkmcnt(0)
	s_barrier
	ds_read_b128 v[156:159], v147
	ds_read_b32 v137, v134 offset:128
	s_waitcnt lgkmcnt(1)
	v_mfma_f32_16x16x32_f16 v[130:133], v[156:159], v[2:5], v[130:133]
	v_mfma_f32_16x16x32_f16 v[152:155], v[156:159], v[22:25], v[152:155]
	s_nop 7
	v_cndmask_b32_e64 v156, v130, v152, s[0:1]
	v_exp_f32_e64 v158, -|v156|
	v_max_f32 v159, 0, v156
	v_add_f32 v158, 1.0, v158
	v_log_f32 v158, v158
	s_nop 0
	v_fma_mixlo_f16 v157, v158, 1.0, v159
	ds_write_b16 v148, v157
	v_mov_b32_e32 v192, v106
	v_mov_b32_e32 v193, 0
	v_mov_b32_e32 v196, v110
	v_mov_b32_e32 v197, 0
	v_mul_f32 v136, -2.0, v137
	s_waitcnt lgkmcnt(0)
	s_barrier
	ds_read_b128 v[216:219], v139
	s_nop 4
	ds_read_b128 v[220:223], v141
	s_waitcnt lgkmcnt(1)
	v_smfmac_f32_16x16x64_f16 v[192:195], v[216:219], v[6:13], v191
	v_smfmac_f32_16x16x64_f16 v[196:199], v[216:219], v[26:33], v191
	s_waitcnt lgkmcnt(0)
	v_smfmac_f32_16x16x64_f16 v[192:195], v[220:223], v[14:21], v191
	v_smfmac_f32_16x16x64_f16 v[196:199], v[220:223], v[34:41], v191
	s_nop 6
	v_add_f32_e32 v224, v192, v193
	v_add_f32_e32 v225, v196, v197
	v_cndmask_b32_e64 v156, v224, v225, s[0:1]
	v_exp_f32_e64 v158, -|v156|
	v_max_f32 v159, 0, v156
	v_add_f32 v158, 1.0, v158
	v_log_f32 v158, v158
	s_nop 0
	v_fma_mixlo_f16 v157, v158, 1.0, v159
	ds_write_b16 v149, v157
	v_mov_b32_e32 v200, v114
	v_mov_b32_e32 v201, 0
	v_mov_b32_e32 v204, v118
	v_mov_b32_e32 v205, 0
	v_mov_b32_e32 v208, v122
	v_mov_b32_e32 v209, 0
	v_mov_b32_e32 v212, v126
	v_mov_b32_e32 v213, 0
	s_waitcnt lgkmcnt(0)
	s_barrier
	ds_read_b128 v[216:219], v143
	s_nop 4
	ds_read_b128 v[220:223], v145
	s_waitcnt lgkmcnt(1)
	v_smfmac_f32_16x16x64_f16 v[200:203], v[216:219], v[42:49], v191
	v_smfmac_f32_16x16x64_f16 v[204:207], v[216:219], v[58:65], v191
	v_smfmac_f32_16x16x64_f16 v[208:211], v[216:219], v[74:81], v191
	v_smfmac_f32_16x16x64_f16 v[212:215], v[216:219], v[90:97], v191
	s_waitcnt lgkmcnt(0)
	v_smfmac_f32_16x16x64_f16 v[200:203], v[220:223], v[50:57], v191
	v_smfmac_f32_16x16x64_f16 v[204:207], v[220:223], v[66:73], v191
	v_smfmac_f32_16x16x64_f16 v[208:211], v[220:223], v[82:89], v191
	v_smfmac_f32_16x16x64_f16 v[212:215], v[220:223], v[98:105], v191
	s_nop 4
	v_add_f32_e32 v224, v200, v201
	v_add_f32_e32 v225, v204, v205
	v_add_f32_e32 v226, v208, v209
	v_add_f32_e32 v227, v212, v213
	v_cndmask_b32_e64 v172, v225, v224, s[6:7]
	v_cndmask_b32_e64 v172, v172, v226, s[0:1]
	v_cndmask_b32_e64 v172, v172, v227, s[4:5]
	v_exp_f32_e32 v172, v172
	s_nop 0
	v_add_f32_e32 v172, 1.0, v172
	v_rcp_f32_e32 v172, v172
	s_nop 0
	v_fmac_f32_e32 v137, v172, v136
	s_nop 1
	v_add_f32_dpp v136, v137, v137 quad_perm:[1,0,3,2] row_mask:0xf bank_mask:0xf bound_ctrl:1
	s_nop 1
	v_add_f32_dpp v136, v136, v136 quad_perm:[2,3,0,1] row_mask:0xf bank_mask:0xf bound_ctrl:1
	s_nop 1
	v_add_f32_dpp v136, v136, v136 row_half_mirror row_mask:0xf bank_mask:0xf bound_ctrl:1
	v_cvt_f16_f32_e32 v137, v136
	ds_write_b16 v150, v137
	v_add_f32_e32 v135, v135, v136
	s_waitcnt lgkmcnt(0)
	s_barrier
	ds_read_b128 v[156:159], v147
	ds_read_b32 v137, v134 offset:160
	s_waitcnt lgkmcnt(1)
	v_mfma_f32_16x16x32_f16 v[130:133], v[156:159], v[2:5], v[130:133]
	v_mfma_f32_16x16x32_f16 v[152:155], v[156:159], v[22:25], v[152:155]
	s_nop 7
	v_cndmask_b32_e64 v156, v130, v152, s[0:1]
	v_exp_f32_e64 v158, -|v156|
	v_max_f32 v159, 0, v156
	v_add_f32 v158, 1.0, v158
	v_log_f32 v158, v158
	s_nop 0
	v_fma_mixlo_f16 v157, v158, 1.0, v159
	ds_write_b16 v148, v157
	v_mov_b32_e32 v192, v106
	v_mov_b32_e32 v193, 0
	v_mov_b32_e32 v196, v110
	v_mov_b32_e32 v197, 0
	v_mul_f32 v136, -2.0, v137
	s_waitcnt lgkmcnt(0)
	s_barrier
	ds_read_b128 v[216:219], v139
	s_nop 4
	ds_read_b128 v[220:223], v141
	s_waitcnt lgkmcnt(1)
	v_smfmac_f32_16x16x64_f16 v[192:195], v[216:219], v[6:13], v191
	v_smfmac_f32_16x16x64_f16 v[196:199], v[216:219], v[26:33], v191
	s_waitcnt lgkmcnt(0)
	v_smfmac_f32_16x16x64_f16 v[192:195], v[220:223], v[14:21], v191
	v_smfmac_f32_16x16x64_f16 v[196:199], v[220:223], v[34:41], v191
	s_nop 6
	v_add_f32_e32 v224, v192, v193
	v_add_f32_e32 v225, v196, v197
	v_cndmask_b32_e64 v156, v224, v225, s[0:1]
	v_exp_f32_e64 v158, -|v156|
	v_max_f32 v159, 0, v156
	v_add_f32 v158, 1.0, v158
	v_log_f32 v158, v158
	s_nop 0
	v_fma_mixlo_f16 v157, v158, 1.0, v159
	ds_write_b16 v149, v157
	v_mov_b32_e32 v200, v114
	v_mov_b32_e32 v201, 0
	v_mov_b32_e32 v204, v118
	v_mov_b32_e32 v205, 0
	v_mov_b32_e32 v208, v122
	v_mov_b32_e32 v209, 0
	v_mov_b32_e32 v212, v126
	v_mov_b32_e32 v213, 0
	s_waitcnt lgkmcnt(0)
	s_barrier
	ds_read_b128 v[216:219], v143
	s_nop 4
	ds_read_b128 v[220:223], v145
	s_waitcnt lgkmcnt(1)
	v_smfmac_f32_16x16x64_f16 v[200:203], v[216:219], v[42:49], v191
	v_smfmac_f32_16x16x64_f16 v[204:207], v[216:219], v[58:65], v191
	v_smfmac_f32_16x16x64_f16 v[208:211], v[216:219], v[74:81], v191
	v_smfmac_f32_16x16x64_f16 v[212:215], v[216:219], v[90:97], v191
	s_waitcnt lgkmcnt(0)
	v_smfmac_f32_16x16x64_f16 v[200:203], v[220:223], v[50:57], v191
	v_smfmac_f32_16x16x64_f16 v[204:207], v[220:223], v[66:73], v191
	v_smfmac_f32_16x16x64_f16 v[208:211], v[220:223], v[82:89], v191
	v_smfmac_f32_16x16x64_f16 v[212:215], v[220:223], v[98:105], v191
	s_nop 4
	v_add_f32_e32 v224, v200, v201
	v_add_f32_e32 v225, v204, v205
	v_add_f32_e32 v226, v208, v209
	v_add_f32_e32 v227, v212, v213
	v_cndmask_b32_e64 v172, v225, v224, s[6:7]
	v_cndmask_b32_e64 v172, v172, v226, s[0:1]
	v_cndmask_b32_e64 v172, v172, v227, s[4:5]
	v_exp_f32_e32 v172, v172
	s_nop 0
	v_add_f32_e32 v172, 1.0, v172
	v_rcp_f32_e32 v172, v172
	s_nop 0
	v_fmac_f32_e32 v137, v172, v136
	s_nop 1
	v_add_f32_dpp v136, v137, v137 quad_perm:[1,0,3,2] row_mask:0xf bank_mask:0xf bound_ctrl:1
	s_nop 1
	v_add_f32_dpp v136, v136, v136 quad_perm:[2,3,0,1] row_mask:0xf bank_mask:0xf bound_ctrl:1
	s_nop 1
	v_add_f32_dpp v136, v136, v136 row_half_mirror row_mask:0xf bank_mask:0xf bound_ctrl:1
	v_cvt_f16_f32_e32 v137, v136
	ds_write_b16 v150, v137
	v_add_f32_e32 v135, v135, v136
	s_waitcnt lgkmcnt(0)
	s_barrier
	ds_read_b128 v[156:159], v147
	ds_read_b32 v137, v134 offset:192
	s_waitcnt lgkmcnt(1)
	v_mfma_f32_16x16x32_f16 v[130:133], v[156:159], v[2:5], v[130:133]
	v_mfma_f32_16x16x32_f16 v[154:157], v[156:159], v[22:25], v[152:155]
	s_nop 7
	v_cndmask_b32_e64 v152, v130, v154, s[0:1]
	v_exp_f32_e64 v158, -|v152|
	v_max_f32 v159, 0, v152
	v_add_f32 v158, 1.0, v158
	v_log_f32 v158, v158
	s_nop 0
	v_fma_mixlo_f16 v153, v158, 1.0, v159
	ds_write_b16 v148, v153
	v_mov_b32_e32 v192, v106
	v_mov_b32_e32 v193, 0
	v_mov_b32_e32 v196, v110
	v_mov_b32_e32 v197, 0
	v_mul_f32 v136, -2.0, v137
	s_waitcnt lgkmcnt(0)
	s_barrier
	ds_read_b128 v[216:219], v139
	s_nop 4
	ds_read_b128 v[220:223], v141
	s_waitcnt lgkmcnt(1)
	v_smfmac_f32_16x16x64_f16 v[192:195], v[216:219], v[6:13], v191
	v_smfmac_f32_16x16x64_f16 v[196:199], v[216:219], v[26:33], v191
	s_waitcnt lgkmcnt(0)
	v_smfmac_f32_16x16x64_f16 v[192:195], v[220:223], v[14:21], v191
	v_smfmac_f32_16x16x64_f16 v[196:199], v[220:223], v[34:41], v191
	s_nop 6
	v_add_f32_e32 v224, v192, v193
	v_add_f32_e32 v225, v196, v197
	v_cndmask_b32_e64 v152, v224, v225, s[0:1]
	v_exp_f32_e64 v158, -|v152|
	v_max_f32 v159, 0, v152
	v_add_f32 v158, 1.0, v158
	v_log_f32 v158, v158
	s_nop 0
	v_fma_mixlo_f16 v153, v158, 1.0, v159
	ds_write_b16 v149, v153
	v_mov_b32_e32 v200, v114
	v_mov_b32_e32 v201, 0
	v_mov_b32_e32 v204, v118
	v_mov_b32_e32 v205, 0
	v_mov_b32_e32 v208, v122
	v_mov_b32_e32 v209, 0
	v_mov_b32_e32 v212, v126
	v_mov_b32_e32 v213, 0
	s_waitcnt lgkmcnt(0)
	s_barrier
	ds_read_b128 v[216:219], v143
	s_nop 4
	ds_read_b128 v[220:223], v145
	s_waitcnt lgkmcnt(1)
	v_smfmac_f32_16x16x64_f16 v[200:203], v[216:219], v[42:49], v191
	v_smfmac_f32_16x16x64_f16 v[204:207], v[216:219], v[58:65], v191
	v_smfmac_f32_16x16x64_f16 v[208:211], v[216:219], v[74:81], v191
	v_smfmac_f32_16x16x64_f16 v[212:215], v[216:219], v[90:97], v191
	s_waitcnt lgkmcnt(0)
	v_smfmac_f32_16x16x64_f16 v[200:203], v[220:223], v[50:57], v191
	v_smfmac_f32_16x16x64_f16 v[204:207], v[220:223], v[66:73], v191
	v_smfmac_f32_16x16x64_f16 v[208:211], v[220:223], v[82:89], v191
	v_smfmac_f32_16x16x64_f16 v[212:215], v[220:223], v[98:105], v191
	s_nop 4
	v_add_f32_e32 v224, v200, v201
	v_add_f32_e32 v225, v204, v205
	v_add_f32_e32 v226, v208, v209
	v_add_f32_e32 v227, v212, v213
	v_cndmask_b32_e64 v152, v225, v224, s[6:7]
	v_cndmask_b32_e64 v152, v152, v226, s[0:1]
	v_cndmask_b32_e64 v152, v152, v227, s[4:5]
	v_exp_f32_e32 v152, v152
	s_nop 0
	v_add_f32_e32 v152, 1.0, v152
	v_rcp_f32_e32 v152, v152
	s_nop 0
	v_fmac_f32_e32 v137, v152, v136
	s_nop 1
	v_add_f32_dpp v136, v137, v137 quad_perm:[1,0,3,2] row_mask:0xf bank_mask:0xf bound_ctrl:1
	s_nop 1
	v_add_f32_dpp v136, v136, v136 quad_perm:[2,3,0,1] row_mask:0xf bank_mask:0xf bound_ctrl:1
	s_nop 1
	v_add_f32_dpp v136, v136, v136 row_half_mirror row_mask:0xf bank_mask:0xf bound_ctrl:1
	v_cvt_f16_f32_e32 v137, v136
	ds_write_b16 v150, v137
	v_add_f32_e32 v152, v135, v136
	s_waitcnt lgkmcnt(0)
	s_barrier
	ds_read_b128 v[158:161], v147
	ds_read_b32 v153, v134 offset:224
	s_addk_i32 s3, 0x100
	s_cmpk_eq_u32 s3, 0xfa20
	s_waitcnt lgkmcnt(1)
	v_mfma_f32_16x16x32_f16 v[130:133], v[158:161], v[2:5], v[130:133]
	v_mfma_f32_16x16x32_f16 v[134:137], v[158:161], v[22:25], v[154:157]
	s_nop 7
	v_cndmask_b32_e64 v154, v130, v134, s[0:1]
	s_cbranch_scc0 .LBB0_21
	s_and_saveexec_b64 s[0:1], vcc
	ds_write_b32 v1, v152
	s_or_b64 exec, exec, s[0:1]
	v_cmp_gt_u32_e32 vcc, 10, v0
	s_waitcnt lgkmcnt(0)
	s_barrier
	s_and_saveexec_b64 s[0:1], vcc
	s_cbranch_execz .LBB0_28
	v_lshlrev_b32_e32 v1, 2, v0
	global_load_dword v1, v1, s[12:13]
	v_mov_b32_e32 v139, 0
	v_lshl_add_u64 v[2:3], s[10:11], 0, v[138:139]
	v_lshl_add_u64 v[2:3], v[2:3], 0, 28
	s_mov_b32 s0, 0
